# moe_layout: the eight expert-counter loads issued together (one round trip instead of four) at the start of P11-P14
# speedup vs baseline: 1.0051x; 1.0051x over previous
.LBB0_1770:
	s_cmp_lt_i32 s92, 12
	s_cselect_b64 s[2:3], -1, 0
	s_and_b64 s[2:3], s[2:3], s[0:1]
	s_andn2_b64 vcc, exec, s[2:3]
	s_cbranch_vccnz .LBB0_1780
	v_mbcnt_lo_u32_b32 v0, -1, 0
	v_mbcnt_hi_u32_b32 v0, -1, v0
	s_nop 0
	v_sub_u32_e32 v0, 0, v0
	v_cmp_eq_u32_e32 vcc, s79, v0
	s_and_saveexec_b64 s[0:1], vcc
	s_cbranch_execz .LBB0_1773
	s_add_i32 s4, 0, 0x23980
	v_mov_b32_e32 v0, 0
	v_mov_b32_e32 v2, s4
	s_add_i32 s4, 0, 0x239c0
	s_waitcnt lgkmcnt(0)
	global_load_dword v10, v0, s[66:67] offset:256 sc1
	global_load_dword v11, v0, s[66:67] offset:260 sc1
	global_load_dword v12, v0, s[66:67] offset:264 sc1
	global_load_dword v13, v0, s[66:67] offset:268 sc1
	global_load_dword v14, v0, s[66:67] offset:272 sc1
	global_load_dword v15, v0, s[66:67] offset:276 sc1
	global_load_dword v16, v0, s[66:67] offset:280 sc1
	global_load_dword v17, v0, s[66:67] offset:284 sc1
	s_waitcnt vmcnt(0)
	v_mov_b32_e32 v1, v10
	ds_write_b32 v2, v0
	v_mov_b32_e32 v2, s4
	ds_write_b32 v2, v0
	v_mov_b32_e32 v2, v11
	s_add_i32 s4, 0, 0x23984
	s_add_i32 s5, 0, 0x239c4
	v_mov_b32_e32 v3, s4
	s_add_i32 s6, 0, 0x23988
	s_waitcnt vmcnt(0)
	v_mov_b32_e32 v4, s5
	s_add_i32 s7, 0, 0x239c8
	v_mov_b32_e32 v5, s6
	v_mov_b32_e32 v6, s7
	s_add_i32 s4, 0, 0x2398c
	s_add_i32 s5, 0, 0x239cc
	s_add_i32 s6, 0, 0x23990
	s_add_i32 s7, 0, 0x239d0
	v_mov_b32_e32 v8, s7
	s_add_i32 s7, 0, 0x239d8
	v_add_u32_e32 v1, 0xff, v1
	v_lshrrev_b32_e32 v7, 8, v1
	v_and_b32_e32 v1, 0xffffff00, v1
	ds_write_b32 v3, v1
	ds_write_b32 v4, v7
	v_add_u32_e32 v2, 0xff, v2
	v_lshrrev_b32_e32 v3, 8, v2
	v_and_b32_e32 v2, 0xffffff00, v2
	v_mov_b32_e32 v4, v12
	v_add_u32_e32 v1, v2, v1
	v_add_u32_e32 v2, v3, v7
	ds_write_b32 v5, v1
	ds_write_b32 v6, v2
	v_mov_b32_e32 v3, v13
	v_mov_b32_e32 v5, s4
	v_mov_b32_e32 v6, s5
	v_mov_b32_e32 v7, s6
	s_add_i32 s4, 0, 0x23994
	s_add_i32 s5, 0, 0x239d4
	s_add_i32 s6, 0, 0x23998
	s_waitcnt vmcnt(1)
	v_add_u32_e32 v4, 0xff, v4
	v_lshrrev_b32_e32 v9, 8, v4
	v_and_b32_e32 v4, 0xffffff00, v4
	v_add_u32_e32 v1, v4, v1
	s_waitcnt vmcnt(0)
	v_add_u32_e32 v3, 0xff, v3
	v_add_u32_e32 v2, v9, v2
	ds_write_b32 v5, v1
	ds_write_b32 v6, v2
	v_lshrrev_b32_e32 v4, 8, v3
	v_and_b32_e32 v3, 0xffffff00, v3
	v_mov_b32_e32 v5, v14
	v_add_u32_e32 v1, v3, v1
	v_add_u32_e32 v2, v4, v2
	ds_write_b32 v7, v1
	ds_write_b32 v8, v2
	v_mov_b32_e32 v3, v15
	v_mov_b32_e32 v4, s4
	v_mov_b32_e32 v6, s5
	v_mov_b32_e32 v7, s6
	v_mov_b32_e32 v8, s7
	s_add_i32 s4, 0, 0x2399c
	s_add_i32 s5, 0, 0x239dc
	s_add_i32 s6, 0, 0x239a0
	s_add_i32 s7, 0, 0x239e0
	s_waitcnt vmcnt(1)
	v_add_u32_e32 v5, 0xff, v5
	v_lshrrev_b32_e32 v9, 8, v5
	v_and_b32_e32 v5, 0xffffff00, v5
	v_add_u32_e32 v1, v5, v1
	s_waitcnt vmcnt(0)
	v_add_u32_e32 v3, 0xff, v3
	v_add_u32_e32 v2, v9, v2
	ds_write_b32 v4, v1
	ds_write_b32 v6, v2
	v_lshrrev_b32_e32 v4, 8, v3
	v_and_b32_e32 v3, 0xffffff00, v3
	v_mov_b32_e32 v5, v16
	v_add_u32_e32 v1, v3, v1
	v_add_u32_e32 v2, v4, v2
	ds_write_b32 v7, v1
	ds_write_b32 v8, v2
	v_mov_b32_e32 v0, v17
	v_mov_b32_e32 v3, s4
	v_mov_b32_e32 v4, s5
	v_mov_b32_e32 v6, s6
	v_mov_b32_e32 v7, s7
	s_waitcnt vmcnt(1)
	v_add_u32_e32 v5, 0xff, v5
	v_lshrrev_b32_e32 v8, 8, v5
	v_and_b32_e32 v5, 0xffffff00, v5
	v_add_u32_e32 v1, v5, v1
	s_waitcnt vmcnt(0)
	v_add_u32_e32 v0, 0xff, v0
	v_add_u32_e32 v2, v8, v2
	ds_write_b32 v3, v1
	ds_write_b32 v4, v2
	v_lshrrev_b32_e32 v3, 8, v0
	v_and_b32_e32 v0, 0xffffff00, v0
	v_add_u32_e32 v0, v0, v1
	v_add_u32_e32 v1, v3, v2
	ds_write_b32 v6, v0
	ds_write_b32 v7, v1

.LBB0_1836:
	s_cmp_lt_i32 s92, 13
	s_cselect_b64 s[2:3], -1, 0
	s_and_b64 s[2:3], s[2:3], s[0:1]
	s_andn2_b64 vcc, exec, s[2:3]
	s_cbranch_vccnz .LBB0_1855
	v_mbcnt_lo_u32_b32 v0, -1, 0
	v_mbcnt_hi_u32_b32 v0, -1, v0
	s_nop 0
	v_sub_u32_e32 v0, 0, v0
	v_cmp_eq_u32_e32 vcc, s79, v0
	s_and_saveexec_b64 s[0:1], vcc
	s_cbranch_execz .LBB0_1839
	s_add_i32 s4, 0, 0x23980
	v_mov_b32_e32 v0, 0
	v_mov_b32_e32 v2, s4
	s_add_i32 s4, 0, 0x239c0
	s_waitcnt lgkmcnt(0)
	global_load_dword v10, v0, s[66:67] offset:256 sc1
	global_load_dword v11, v0, s[66:67] offset:260 sc1
	global_load_dword v12, v0, s[66:67] offset:264 sc1
	global_load_dword v13, v0, s[66:67] offset:268 sc1
	global_load_dword v14, v0, s[66:67] offset:272 sc1
	global_load_dword v15, v0, s[66:67] offset:276 sc1
	global_load_dword v16, v0, s[66:67] offset:280 sc1
	global_load_dword v17, v0, s[66:67] offset:284 sc1
	s_waitcnt vmcnt(0)
	v_mov_b32_e32 v1, v10
	ds_write_b32 v2, v0
	v_mov_b32_e32 v2, s4
	ds_write_b32 v2, v0
	v_mov_b32_e32 v2, v11
	s_add_i32 s4, 0, 0x23984
	s_add_i32 s5, 0, 0x239c4
	v_mov_b32_e32 v3, s4
	s_add_i32 s6, 0, 0x23988
	s_waitcnt vmcnt(0)
	v_mov_b32_e32 v4, s5
	s_add_i32 s7, 0, 0x239c8
	v_mov_b32_e32 v5, s6
	v_mov_b32_e32 v6, s7
	s_add_i32 s4, 0, 0x2398c
	s_add_i32 s5, 0, 0x239cc
	s_add_i32 s6, 0, 0x23990
	s_add_i32 s7, 0, 0x239d0
	v_mov_b32_e32 v8, s7
	s_add_i32 s7, 0, 0x239d8
	v_add_u32_e32 v1, 0xff, v1
	v_lshrrev_b32_e32 v7, 8, v1
	v_and_b32_e32 v1, 0xffffff00, v1
	ds_write_b32 v3, v1
	ds_write_b32 v4, v7
	v_add_u32_e32 v2, 0xff, v2
	v_lshrrev_b32_e32 v3, 8, v2
	v_and_b32_e32 v2, 0xffffff00, v2
	v_mov_b32_e32 v4, v12
	v_add_u32_e32 v1, v2, v1
	v_add_u32_e32 v2, v3, v7
	ds_write_b32 v5, v1
	ds_write_b32 v6, v2
	v_mov_b32_e32 v3, v13
	v_mov_b32_e32 v5, s4
	v_mov_b32_e32 v6, s5
	v_mov_b32_e32 v7, s6
	s_add_i32 s4, 0, 0x23994
	s_add_i32 s5, 0, 0x239d4
	s_add_i32 s6, 0, 0x23998
	s_waitcnt vmcnt(1)
	v_add_u32_e32 v4, 0xff, v4
	v_lshrrev_b32_e32 v9, 8, v4
	v_and_b32_e32 v4, 0xffffff00, v4
	v_add_u32_e32 v1, v4, v1
	s_waitcnt vmcnt(0)
	v_add_u32_e32 v3, 0xff, v3
	v_add_u32_e32 v2, v9, v2
	ds_write_b32 v5, v1
	ds_write_b32 v6, v2
	v_lshrrev_b32_e32 v4, 8, v3
	v_and_b32_e32 v3, 0xffffff00, v3
	v_mov_b32_e32 v5, v14
	v_add_u32_e32 v1, v3, v1
	v_add_u32_e32 v2, v4, v2
	ds_write_b32 v7, v1
	ds_write_b32 v8, v2
	v_mov_b32_e32 v3, v15
	v_mov_b32_e32 v4, s4
	v_mov_b32_e32 v6, s5
	v_mov_b32_e32 v7, s6
	v_mov_b32_e32 v8, s7
	s_add_i32 s4, 0, 0x2399c
	s_add_i32 s5, 0, 0x239dc
	s_add_i32 s6, 0, 0x239a0
	s_add_i32 s7, 0, 0x239e0
	s_waitcnt vmcnt(1)
	v_add_u32_e32 v5, 0xff, v5
	v_lshrrev_b32_e32 v9, 8, v5
	v_and_b32_e32 v5, 0xffffff00, v5
	v_add_u32_e32 v1, v5, v1
	s_waitcnt vmcnt(0)
	v_add_u32_e32 v3, 0xff, v3
	v_add_u32_e32 v2, v9, v2
	ds_write_b32 v4, v1
	ds_write_b32 v6, v2
	v_lshrrev_b32_e32 v4, 8, v3
	v_and_b32_e32 v3, 0xffffff00, v3
	v_mov_b32_e32 v5, v16
	v_add_u32_e32 v1, v3, v1
	v_add_u32_e32 v2, v4, v2
	ds_write_b32 v7, v1
	ds_write_b32 v8, v2
	v_mov_b32_e32 v0, v17
	v_mov_b32_e32 v3, s4
	v_mov_b32_e32 v4, s5
	v_mov_b32_e32 v6, s6
	v_mov_b32_e32 v7, s7
	s_waitcnt vmcnt(1)
	v_add_u32_e32 v5, 0xff, v5
	v_lshrrev_b32_e32 v8, 8, v5
	v_and_b32_e32 v5, 0xffffff00, v5
	v_add_u32_e32 v1, v5, v1
	s_waitcnt vmcnt(0)
	v_add_u32_e32 v0, 0xff, v0
	v_add_u32_e32 v2, v8, v2
	ds_write_b32 v3, v1
	ds_write_b32 v4, v2
	v_lshrrev_b32_e32 v3, 8, v0
	v_and_b32_e32 v0, 0xffffff00, v0
	v_add_u32_e32 v0, v0, v1
	v_add_u32_e32 v1, v3, v2
	ds_write_b32 v6, v0
	ds_write_b32 v7, v1

.LBB0_1911:
	s_cmp_lt_i32 s92, 14
	s_cselect_b64 s[2:3], -1, 0
	s_and_b64 s[2:3], s[2:3], s[0:1]
	s_andn2_b64 vcc, exec, s[2:3]
	s_cbranch_vccnz .LBB0_1930
	v_mbcnt_lo_u32_b32 v0, -1, 0
	v_mbcnt_hi_u32_b32 v0, -1, v0
	s_nop 0
	v_sub_u32_e32 v0, 0, v0
	v_cmp_eq_u32_e32 vcc, s79, v0
	s_and_saveexec_b64 s[0:1], vcc
	s_cbranch_execz .LBB0_1914
	s_add_i32 s4, 0, 0x23980
	v_mov_b32_e32 v0, 0
	v_mov_b32_e32 v2, s4
	s_add_i32 s4, 0, 0x239c0
	s_waitcnt lgkmcnt(0)
	global_load_dword v10, v0, s[66:67] offset:256 sc1
	global_load_dword v11, v0, s[66:67] offset:260 sc1
	global_load_dword v12, v0, s[66:67] offset:264 sc1
	global_load_dword v13, v0, s[66:67] offset:268 sc1
	global_load_dword v14, v0, s[66:67] offset:272 sc1
	global_load_dword v15, v0, s[66:67] offset:276 sc1
	global_load_dword v16, v0, s[66:67] offset:280 sc1
	global_load_dword v17, v0, s[66:67] offset:284 sc1
	s_waitcnt vmcnt(0)
	v_mov_b32_e32 v1, v10
	ds_write_b32 v2, v0
	v_mov_b32_e32 v2, s4
	ds_write_b32 v2, v0
	v_mov_b32_e32 v2, v11
	s_add_i32 s4, 0, 0x23984
	s_add_i32 s5, 0, 0x239c4
	v_mov_b32_e32 v3, s4
	s_add_i32 s6, 0, 0x23988
	s_waitcnt vmcnt(0)
	v_mov_b32_e32 v4, s5
	s_add_i32 s7, 0, 0x239c8
	v_mov_b32_e32 v5, s6
	v_mov_b32_e32 v6, s7
	s_add_i32 s4, 0, 0x2398c
	s_add_i32 s5, 0, 0x239cc
	s_add_i32 s6, 0, 0x23990
	s_add_i32 s7, 0, 0x239d0
	v_mov_b32_e32 v8, s7
	s_add_i32 s7, 0, 0x239d8
	v_add_u32_e32 v1, 0xff, v1
	v_lshrrev_b32_e32 v7, 8, v1
	v_and_b32_e32 v1, 0xffffff00, v1
	ds_write_b32 v3, v1
	ds_write_b32 v4, v7
	v_add_u32_e32 v2, 0xff, v2
	v_lshrrev_b32_e32 v3, 8, v2
	v_and_b32_e32 v2, 0xffffff00, v2
	v_mov_b32_e32 v4, v12
	v_add_u32_e32 v1, v2, v1
	v_add_u32_e32 v2, v3, v7
	ds_write_b32 v5, v1
	ds_write_b32 v6, v2
	v_mov_b32_e32 v3, v13
	v_mov_b32_e32 v5, s4
	v_mov_b32_e32 v6, s5
	v_mov_b32_e32 v7, s6
	s_add_i32 s4, 0, 0x23994
	s_add_i32 s5, 0, 0x239d4
	s_add_i32 s6, 0, 0x23998
	s_waitcnt vmcnt(1)
	v_add_u32_e32 v4, 0xff, v4
	v_lshrrev_b32_e32 v9, 8, v4
	v_and_b32_e32 v4, 0xffffff00, v4
	v_add_u32_e32 v1, v4, v1
	s_waitcnt vmcnt(0)
	v_add_u32_e32 v3, 0xff, v3
	v_add_u32_e32 v2, v9, v2
	ds_write_b32 v5, v1
	ds_write_b32 v6, v2
	v_lshrrev_b32_e32 v4, 8, v3
	v_and_b32_e32 v3, 0xffffff00, v3
	v_mov_b32_e32 v5, v14
	v_add_u32_e32 v1, v3, v1
	v_add_u32_e32 v2, v4, v2
	ds_write_b32 v7, v1
	ds_write_b32 v8, v2
	v_mov_b32_e32 v3, v15
	v_mov_b32_e32 v4, s4
	v_mov_b32_e32 v6, s5
	v_mov_b32_e32 v7, s6
	v_mov_b32_e32 v8, s7
	s_add_i32 s4, 0, 0x2399c
	s_add_i32 s5, 0, 0x239dc
	s_add_i32 s6, 0, 0x239a0
	s_add_i32 s7, 0, 0x239e0
	s_waitcnt vmcnt(1)
	v_add_u32_e32 v5, 0xff, v5
	v_lshrrev_b32_e32 v9, 8, v5
	v_and_b32_e32 v5, 0xffffff00, v5
	v_add_u32_e32 v1, v5, v1
	s_waitcnt vmcnt(0)
	v_add_u32_e32 v3, 0xff, v3
	v_add_u32_e32 v2, v9, v2
	ds_write_b32 v4, v1
	ds_write_b32 v6, v2
	v_lshrrev_b32_e32 v4, 8, v3
	v_and_b32_e32 v3, 0xffffff00, v3
	v_mov_b32_e32 v5, v16
	v_add_u32_e32 v1, v3, v1
	v_add_u32_e32 v2, v4, v2
	ds_write_b32 v7, v1
	ds_write_b32 v8, v2
	v_mov_b32_e32 v0, v17
	v_mov_b32_e32 v3, s4
	v_mov_b32_e32 v4, s5
	v_mov_b32_e32 v6, s6
	v_mov_b32_e32 v7, s7
	s_waitcnt vmcnt(1)
	v_add_u32_e32 v5, 0xff, v5
	v_lshrrev_b32_e32 v8, 8, v5
	v_and_b32_e32 v5, 0xffffff00, v5
	v_add_u32_e32 v1, v5, v1
	s_waitcnt vmcnt(0)
	v_add_u32_e32 v0, 0xff, v0
	v_add_u32_e32 v2, v8, v2
	ds_write_b32 v3, v1
	ds_write_b32 v4, v2
	v_lshrrev_b32_e32 v3, 8, v0
	v_and_b32_e32 v0, 0xffffff00, v0
	v_add_u32_e32 v0, v0, v1
	v_add_u32_e32 v1, v3, v2
	ds_write_b32 v6, v0
	ds_write_b32 v7, v1

.LBB0_1986:
	s_cmp_lt_i32 s92, 15
	s_cselect_b64 s[2:3], -1, 0
	s_and_b64 s[4:5], s[2:3], s[0:1]
	s_andn2_b64 vcc, exec, s[4:5]
	s_cbranch_vccnz .LBB0_2014
	v_mbcnt_lo_u32_b32 v0, -1, 0
	v_mbcnt_hi_u32_b32 v0, -1, v0
	s_nop 0
	v_sub_u32_e32 v0, 0, v0
	v_cmp_eq_u32_e32 vcc, s79, v0
	s_and_saveexec_b64 s[0:1], vcc
	s_cbranch_execz .LBB0_1989
	s_add_i32 s2, 0, 0x23980
	v_mov_b32_e32 v0, 0
	v_mov_b32_e32 v2, s2
	s_add_i32 s2, 0, 0x239c0
	s_waitcnt lgkmcnt(0)
	global_load_dword v10, v0, s[66:67] offset:256 sc1
	global_load_dword v11, v0, s[66:67] offset:260 sc1
	global_load_dword v12, v0, s[66:67] offset:264 sc1
	global_load_dword v13, v0, s[66:67] offset:268 sc1
	global_load_dword v14, v0, s[66:67] offset:272 sc1
	global_load_dword v15, v0, s[66:67] offset:276 sc1
	global_load_dword v16, v0, s[66:67] offset:280 sc1
	global_load_dword v17, v0, s[66:67] offset:284 sc1
	s_waitcnt vmcnt(0)
	v_mov_b32_e32 v1, v10
	ds_write_b32 v2, v0
	v_mov_b32_e32 v2, s2
	ds_write_b32 v2, v0
	v_mov_b32_e32 v2, v11
	s_add_i32 s2, 0, 0x23984
	s_add_i32 s3, 0, 0x239c4
	v_mov_b32_e32 v3, s2
	s_add_i32 s6, 0, 0x23988
	s_waitcnt vmcnt(0)
	v_mov_b32_e32 v4, s3
	s_add_i32 s7, 0, 0x239c8
	v_mov_b32_e32 v5, s6
	v_mov_b32_e32 v6, s7
	s_add_i32 s2, 0, 0x2398c
	s_add_i32 s3, 0, 0x239cc
	s_add_i32 s6, 0, 0x23990
	s_add_i32 s7, 0, 0x239d0
	v_mov_b32_e32 v8, s7
	s_add_i32 s7, 0, 0x239d8
	v_add_u32_e32 v1, 0xff, v1
	v_lshrrev_b32_e32 v7, 8, v1
	v_and_b32_e32 v1, 0xffffff00, v1
	ds_write_b32 v3, v1
	ds_write_b32 v4, v7
	v_add_u32_e32 v2, 0xff, v2
	v_lshrrev_b32_e32 v3, 8, v2
	v_and_b32_e32 v2, 0xffffff00, v2
	v_mov_b32_e32 v4, v12
	v_add_u32_e32 v1, v2, v1
	v_add_u32_e32 v2, v3, v7
	ds_write_b32 v5, v1
	ds_write_b32 v6, v2
	v_mov_b32_e32 v3, v13
	v_mov_b32_e32 v5, s2
	v_mov_b32_e32 v6, s3
	v_mov_b32_e32 v7, s6
	s_add_i32 s2, 0, 0x23994
	s_add_i32 s3, 0, 0x239d4
	s_add_i32 s6, 0, 0x23998
	s_waitcnt vmcnt(1)
	v_add_u32_e32 v4, 0xff, v4
	v_lshrrev_b32_e32 v9, 8, v4
	v_and_b32_e32 v4, 0xffffff00, v4
	v_add_u32_e32 v1, v4, v1
	s_waitcnt vmcnt(0)
	v_add_u32_e32 v3, 0xff, v3
	v_add_u32_e32 v2, v9, v2
	ds_write_b32 v5, v1
	ds_write_b32 v6, v2
	v_lshrrev_b32_e32 v4, 8, v3
	v_and_b32_e32 v3, 0xffffff00, v3
	v_mov_b32_e32 v5, v14
	v_add_u32_e32 v1, v3, v1
	v_add_u32_e32 v2, v4, v2
	ds_write_b32 v7, v1
	ds_write_b32 v8, v2
	v_mov_b32_e32 v3, v15
	v_mov_b32_e32 v4, s2
	v_mov_b32_e32 v6, s3
	v_mov_b32_e32 v7, s6
	v_mov_b32_e32 v8, s7
	s_add_i32 s2, 0, 0x2399c
	s_add_i32 s3, 0, 0x239dc
	s_add_i32 s6, 0, 0x239a0
	s_add_i32 s7, 0, 0x239e0
	s_waitcnt vmcnt(1)
	v_add_u32_e32 v5, 0xff, v5
	v_lshrrev_b32_e32 v9, 8, v5
	v_and_b32_e32 v5, 0xffffff00, v5
	v_add_u32_e32 v1, v5, v1
	s_waitcnt vmcnt(0)
	v_add_u32_e32 v3, 0xff, v3
	v_add_u32_e32 v2, v9, v2
	ds_write_b32 v4, v1
	ds_write_b32 v6, v2
	v_lshrrev_b32_e32 v4, 8, v3
	v_and_b32_e32 v3, 0xffffff00, v3
	v_mov_b32_e32 v5, v16
	v_add_u32_e32 v1, v3, v1
	v_add_u32_e32 v2, v4, v2
	ds_write_b32 v7, v1
	ds_write_b32 v8, v2
	v_mov_b32_e32 v0, v17
	v_mov_b32_e32 v3, s2
	v_mov_b32_e32 v4, s3
	v_mov_b32_e32 v6, s6
	v_mov_b32_e32 v7, s7
	s_waitcnt vmcnt(1)
	v_add_u32_e32 v5, 0xff, v5
	v_lshrrev_b32_e32 v8, 8, v5
	v_and_b32_e32 v5, 0xffffff00, v5
	v_add_u32_e32 v1, v5, v1
	s_waitcnt vmcnt(0)
	v_add_u32_e32 v0, 0xff, v0
	v_add_u32_e32 v2, v8, v2
	ds_write_b32 v3, v1
	ds_write_b32 v4, v2
	v_lshrrev_b32_e32 v3, 8, v0
	v_and_b32_e32 v0, 0xffffff00, v0
	v_add_u32_e32 v0, v0, v1
	v_add_u32_e32 v1, v3, v2
	ds_write_b32 v6, v0
	ds_write_b32 v7, v1
